# RWKV waves at issue priority 1 (between the mLSTM waves at 3 and the converter waves at 0)
# speedup vs baseline: 1.0152x; 1.0072x over previous
; #define LAS __attribute__((address_space(3)))
; __device__ __forceinline__ void rwkv_chunk_unit(Frame& F, int unit, LAS unsigned char* regB, LAS unsigned* bcnt, unsigned& btarget) {
;     const int b = unit >> 5, h = (unit >> 1) & 15, half = unit & 1;
;     const bf16* P = (const bf16*)(F.ws + WS_P); const float* WAG = (const float*)(F.ws + WS_WAG); const bf16* AGp = (const bf16*)(F.ws + WS_WAG + 64 * MiB); float* YRAW = (float*)(F.ws + WS_YRAW);
;     constexpr int KS = 72, LS = 40;
;     LAS bf16* At = (LAS bf16*)F.lds; LAS bf16* Bt = At + 32 * KS; LAS bf16* Kt = Bt + 32 * KS; LAS bf16* Rt = Kt + 32 * KS;
;     LAS bf16* Vv = Rt + 32 * KS;
;     LAS bf16* Sb = Vv + 32 * LS;
;     LAS bf16* G2b = Sb + 32 * KS; LAS bf16* G3b = G2b + 32 * LS; LAS bf16* G4b = G3b + 32 * LS;
;     LAS bf16* Pwb = G4b + 32 * LS;
;     LAS bf16* Acb = Pwb + 2 * 32 * LS;
;     LAS bf16* RHt = (LAS bf16*)regB;
;     LAS bf16* Ubt = RHt + 32 * LS;
;     LAS float* lwf = (LAS float*)(Ubt + 32 * LS);
;     LAS float* csf = lwf + 2048;
;     LAS float* gtf = csf + 2048;
;     LAS float* glf = gtf + 256;
;     const int tid = F.tid, lane = F.lane, w = F.wave, fr = lane & 15, fq = lane >> 4;
;     const int ts = tid >> 4, cs = tid & 15, c0 = h * 64 + 4 * cs;
;     const int sk = tid & 63, sq = tid >> 6;
;     const f32x4 mu_r = *(const f32x4*)(F.in[I_MU] + c0), mu_k = *(const f32x4*)(F.in[I_MU] + 1024 + c0), mu_v = *(const f32x4*)(F.in[I_MU] + 2048 + c0);
;     const f32x4 kkc = *(const f32x4*)(F.in[I_KK] + c0), kac = *(const f32x4*)(F.in[I_KA] + c0), rkc = *(const f32x4*)(F.in[I_RK] + c0);
;     bf16* BON = (bf16*)(F.ws + WS_WAG + 128 * MiB);
;     for (int i = tid; i < 32 * KS; i += 256) Sb[i] = 0;
;     v2u cr[2], ck[2], cv[2], qr[2], qk[2], qv[2]; f32x4 a4[2], ws0, ws1;
;     ...
;     const int mi = w >> 1, nj = w & 1;
;     f32x4 st[2]; st[0] = (f32x4){0.f, 0.f, 0.f, 0.f}; st[1] = st[0];
;     RC_LOAD(0);
;     rw_bar(bcnt, btarget, lane);
.LBB0_964:
	v_writelane_b32 v237, s74, 61
	v_writelane_b32 v236, s93, 30
	v_writelane_b32 v236, s92, 27
	v_writelane_b32 v237, s75, 62
	v_writelane_b32 v237, s76, 63
	s_and_b64 vcc, exec, s[0:1]
	s_nop 0
	v_writelane_b32 v236, s77, 0
	v_writelane_b32 v236, s78, 1
	v_writelane_b32 v236, s79, 2
	v_writelane_b32 v236, s80, 3
	v_writelane_b32 v236, s81, 4
	v_writelane_b32 v236, s82, 5
	v_writelane_b32 v236, s83, 6
	v_writelane_b32 v236, s84, 7
	v_writelane_b32 v236, s85, 8
	v_writelane_b32 v236, s86, 9
	v_writelane_b32 v236, s87, 10
	v_writelane_b32 v236, s88, 11
	v_writelane_b32 v236, s89, 12
	v_writelane_b32 v236, s90, 13
	v_writelane_b32 v236, s91, 14
	s_cbranch_vccz .LBB0_1058
	v_readlane_b32 s0, v237, 61
	s_cmpk_gt_i32 s0, 0xff
	v_readlane_b32 s1, v237, 62
	s_cbranch_scc1 .LBB0_1058
	v_readlane_b32 s0, v237, 63
	v_readlane_b32 s14, v236, 13
	v_readlane_b32 s1, v236, 0
	v_readlane_b32 s15, v236, 14
	s_add_u32 s0, s14, 0x38200000
	v_readlane_b32 s12, v236, 11
	s_addc_u32 s1, s15, 0
	v_readlane_b32 s13, v236, 12
	s_add_u32 s12, s14, 0x4e200000
	v_readlane_b32 s2, v236, 1
	v_readlane_b32 s3, v236, 2
	v_readlane_b32 s4, v236, 3
	v_readlane_b32 s5, v236, 4
	v_readlane_b32 s6, v236, 5
	v_readlane_b32 s7, v236, 6
	v_readlane_b32 s8, v236, 7
	v_readlane_b32 s9, v236, 8
	v_readlane_b32 s10, v236, 9
	v_readlane_b32 s11, v236, 10
	v_writelane_b32 v236, s0, 15
	s_addc_u32 s13, s15, 0
	v_readlane_b32 s16, v237, 0
	v_writelane_b32 v236, s1, 16
	s_add_u32 s0, s14, 0x52200000
	s_addc_u32 s1, s15, 0
	v_writelane_b32 v236, s0, 17
	v_readlane_b32 s24, v237, 8
	v_readlane_b32 s25, v237, 9
	v_writelane_b32 v236, s1, 18
	s_add_u32 s0, s14, 0x5a200000
	v_writelane_b32 v236, s0, 19
	s_addc_u32 s0, s15, 0
	s_mov_b64 s[8:9], s[24:25]
	v_writelane_b32 v236, s0, 20
	s_add_u32 s0, s8, 0x1000
	s_addc_u32 s1, s9, 0
	v_writelane_b32 v236, s0, 21
	s_waitcnt vmcnt(41)
	v_and_b32_e32 v100, 31, v0
	s_waitcnt vmcnt(4)
	v_lshlrev_b32_e32 v5, 8, v100
	v_writelane_b32 v236, s1, 22
	s_add_u32 s0, s8, 0x2000
	s_addc_u32 s1, s9, 0
	v_writelane_b32 v236, s0, 23
	v_and_b32_e32 v96, 32, v162
	v_mov_b32_e32 v97, 0
	v_writelane_b32 v236, s1, 24
	s_add_u32 s0, s14, 0x56200000
	s_addc_u32 s1, s15, 0
	v_writelane_b32 v236, s0, 25
	s_add_i32 s5, 0, 0x23500
	v_and_b32_e32 v2, 15, v0
	v_writelane_b32 v236, s1, 26
	s_waitcnt vmcnt(1)
	v_and_b32_e32 v14, 48, v162
	v_readlane_b32 s14, v236, 27
	s_lshl_b32 s10, s14, 6
	s_lshl_b32 s0, s14, 4
	s_add_i32 s2, s10, s5
	v_add3_u32 v99, s2, v5, v96
	s_add_u32 s2, s12, s10
	v_writelane_b32 v236, s12, 28
	s_addc_u32 s3, s13, 0
	v_lshl_add_u64 v[102:103], s[2:3], 0, v[96:97]
	s_lshl_b32 s2, s14, 5
	s_and_b32 s4, s0, 16
	s_add_i32 s11, s2, 0
	s_lshl_b32 s2, s14, 3
	v_or_b32_e32 v12, s4, v2
	v_writelane_b32 v236, s13, 29
	s_and_b32 s13, s2, 16
	v_mul_u32_u24_e32 v13, 0x48, v12
	s_add_i32 s12, 0, 0x25900
	v_or_b32_e32 v9, s13, v2
	v_lshlrev_b32_e32 v13, 1, v13
	v_readlane_b32 s2, v236, 30
	v_add3_u32 v105, 0, v13, v14
	v_mul_u32_u24_e32 v13, 0x48, v9
	s_cmp_gt_u32 s2, 63
	v_lshl_add_u32 v13, v13, 1, 0
	v_lshlrev_b32_e32 v15, 6, v9
	s_cselect_b64 s[2:3], -1, 0
	s_cmp_lg_u32 s14, 1
	v_lshrrev_b32_e32 v3, 5, v162
	v_add_u32_e32 v168, v13, v14
	v_sub_u32_e32 v13, v13, v15
	v_mul_u32_u24_e32 v15, 0x48, v100
	s_cselect_b64 s[8:9], -1, 0
	s_cmp_eq_u32 s14, 2
	v_lshrrev_b32_e32 v1, 4, v162
	v_lshlrev_b32_e32 v5, 4, v3
	v_lshlrev_b32_e32 v15, 1, v15
	s_cselect_b64 s[38:39], -1, 0
	s_add_i32 s14, s0, 0
	v_lshlrev_b32_e32 v10, 2, v1
	v_lshlrev_b32_e32 v1, 3, v1
	v_add3_u32 v170, 0, v5, v15
	s_movk_i32 s15, 0x50
	v_mov_b32_e32 v5, s14
	v_bfe_u32 v15, v0, 2, 2
	v_mul_u32_u24_e32 v12, 40, v12
	v_or_b32_e32 v11, s4, v10
	v_mad_u32_u24 v5, v100, s15, v5
	v_or_b32_e32 v15, v1, v15
	v_lshlrev_b32_e32 v12, 1, v12
	s_add_i32 s14, 0, 0x20100
	s_add_i32 s15, 0, 0x20b00
	v_lshrrev_b32_e32 v94, 4, v0
	v_lshl_add_u32 v169, v11, 1, v13
	v_and_b32_e32 v17, 12, v163
	v_add_u32_e32 v173, v13, v14
	v_add_u32_e32 v13, s14, v12
	s_lshl_b32 s14, s13, 1
	v_add_u32_e32 v12, s15, v12
	v_or_b32_e32 v104, s13, v10
	v_mul_u32_u24_e32 v10, 0x48, v15
	v_lshlrev_b32_e32 v8, 4, v2
	v_lshlrev_b32_e32 v17, 1, v17
	v_add3_u32 v174, v13, s14, v1
	v_add3_u32 v176, v12, s14, v1
	v_add_u32_e32 v177, v12, v14
	v_lshlrev_b32_e32 v10, 1, v10
	v_add_u32_e32 v12, s11, v1
	v_lshlrev_b32_e32 v1, 8, v94
	v_add_u32_e32 v101, s12, v8
	v_add3_u32 v178, s11, v10, v17
	s_add_i32 s12, s12, s10
	v_add3_u32 v180, s5, v1, v8
	v_mul_u32_u24_e32 v1, 0x48, v94
	v_cmp_eq_u32_e64 s[10:11], 31, v94
	v_add_u32_e32 v98, 16, v94
	v_lshlrev_b32_e32 v6, 3, v2
	v_lshlrev_b32_e32 v1, 1, v1
	v_writelane_b32 v236, s10, 31
	v_add3_u32 v182, 0, v6, v1
	v_lshlrev_b32_e32 v1, 8, v98
	v_writelane_b32 v236, s11, 32
	v_cmp_eq_u32_e64 s[10:11], 31, v98
	v_add3_u32 v183, s5, v1, v8
	v_or_b32_e32 v1, 1, v11
	v_writelane_b32 v236, s10, 33
	v_readlane_b32 s22, v237, 6
	v_readlane_b32 s23, v237, 7
	v_writelane_b32 v236, s11, 34
	v_cmp_lt_u32_e64 s[10:11], v1, v9
	v_or_b32_e32 v1, 2, v11
	v_cmp_gt_u32_e64 s[22:23], v1, v9
	v_writelane_b32 v236, s10, 35
	v_lshlrev_b32_e32 v4, 3, v3
	v_lshlrev_b32_e32 v3, 2, v3
	v_writelane_b32 v236, s11, 36
	v_cmp_lt_u32_e64 s[10:11], v1, v9
	v_or_b32_e32 v1, 3, v11
; #define LAS __attribute__((address_space(3)))
; __device__ __forceinline__ unsigned long long pack4bf(f32x4 v) { return (unsigned long long)pk2(v[0], v[1]) | ((unsigned long long)pk2(v[2], v[3]) << 32); }
; #define MFMA32(a_, b_, c_) __builtin_amdgcn_mfma_f32_32x32x16_bf16((a_), (b_), (c_), 0, 0, 0)
; #define TP_A(k) do { if ((k) == TPROBE / 100) tpA = __builtin_amdgcn_s_memrealtime(); } while (0)
; #define TP_B(k) do { if ((k) == TPROBE % 100) tpB = __builtin_amdgcn_s_memrealtime(); } while (0)
; #define TP_A(k) do {} while (0)
; #define TP_B(k) do {} while (0)
; __device__ __forceinline__ void rwkv_chunk_unit(Frame& F, int unit, LAS unsigned char* regB, LAS unsigned* bcnt, unsigned& btarget) {
;     ...
;           for (int rg_ = 0; rg_ < 4; ++rg_) { const int j = jb + rg_; g2[rg_] = (j < t) ? g2[rg_] : 0.f; g3[rg_] = (j <= t) ? g3[rg_] : 0.f; g4[rg_] = (j <= t) ? g4[rg_] : 0.f; }
;           *(LAS unsigned long long*)(G2b + t * LS + jb) = pack4bf(g2); *(LAS unsigned long long*)(G3b + t * LS + jb) = pack4bf(g3); *(LAS unsigned long long*)(G4b + t * LS + jb) = pack4bf(g4); }
;         { const int tq = lane & 31, hq = lane >> 5;
;           f32x16 Pm, Qm, Aq;
; #pragma unroll
;           for (int i = 0; i < 16; ++i) { Pm[i] = 0.f; Qm[i] = 0.f; }
; #pragma unroll
;           for (int s = 0; s < 4; ++s) { const s16x8 fa = *(const LAS s16x8*)(At + tq * KS + 16 * s + 8 * hq), fb = *(const LAS s16x8*)(Bt + tq * KS + 16 * s + 8 * hq);
;               Pm = MFMA32(fa, fb, Pm); Qm = MFMA32(fb, fa, Qm); }
; #pragma unroll
;           for (int i = 0; i < 16; ++i) { const int r_ = (i & 3) + 8 * (i >> 2) + 4 * hq;
;               Pm[i] = (tq < r_) ? Pm[i] : 0.f;
;               Qm[i] = (r_ < tq) ? Qm[i] : 0.f;
;               Aq[i] = Qm[i] + ((r_ == tq) ? 1.f : 0.f); }
; __global__ void __launch_bounds__(NTHR, 2) mk_fwd(Args args) {
;     ...
;           TP_A(14); TP_A(15); TP_A(16); if (F.wave < 4) { TP_B(14); TP_B(16); unsigned bt = 0u; for (int rep = 0; rep < REP(40); ++rep) for (int u = F.bid; u < 256; u += F.G) rwkv_chunk_unit(F, u, (LAS unsigned char*)F.MISC + 256, ctl2, bt); TP_B(15); }
	v_readlane_b32 s26, v237, 10
	v_writelane_b32 v236, s10, 37
	v_readlane_b32 s27, v237, 11
	v_cmp_gt_u32_e64 s[26:27], v1, v9
	v_writelane_b32 v236, s11, 38
	v_cmp_lt_u32_e64 s[10:11], v1, v9
	v_or_b32_e32 v1, 1, v3
	v_cmp_eq_u32_e32 vcc, v3, v100
	v_writelane_b32 v236, s10, 39
	v_or_b32_e32 v8, 2, v3
	v_cndmask_b32_e64 v185, 0, 1.0, vcc
	v_writelane_b32 v236, s11, 40
	v_cmp_lt_u32_e64 s[10:11], v100, v3
	v_cmp_eq_u32_e32 vcc, v1, v100
	v_cmp_lt_u32_e64 s[34:35], v8, v100
	v_writelane_b32 v236, s10, 41
	v_cndmask_b32_e64 v186, 0, 1.0, vcc
	v_cmp_eq_u32_e32 vcc, v8, v100
	v_writelane_b32 v236, s11, 42
	v_cmp_lt_u32_e64 s[10:11], v1, v100
	v_readlane_b32 s28, v237, 12
	v_readlane_b32 s29, v237, 13
	v_writelane_b32 v236, s10, 43
	v_or_b32_e32 v1, 3, v3
	v_cmp_eq_u32_e64 s[44:45], v1, v100
	v_writelane_b32 v236, s11, 44
	v_cmp_lt_u32_e64 s[10:11], v100, v8
	v_or_b32_e32 v8, 8, v3
	v_cmp_lt_u32_e64 s[24:25], v100, v1
	v_writelane_b32 v236, s10, 45
	v_cmp_lt_u32_e64 s[28:29], v1, v100
	v_or_b32_e32 v1, 9, v3
	v_writelane_b32 v236, s11, 46
	v_cmp_lt_u32_e64 s[10:11], v100, v8
	v_cmp_eq_u32_e64 s[52:53], v1, v100
	v_cndmask_b32_e64 v106, 0, 1.0, vcc
	v_writelane_b32 v236, s10, 47
	v_cmp_eq_u32_e32 vcc, v8, v100
	v_cndmask_b32_e64 v109, 0, 1.0, s[52:53]
	v_writelane_b32 v236, s11, 48
	v_cmp_lt_u32_e64 s[10:11], v100, v1
	v_cndmask_b32_e64 v108, 0, 1.0, vcc
	s_mov_b32 s1, 0
	v_writelane_b32 v236, s10, 49
	s_lshl_b32 s0, s0, 2
	v_readlane_b32 s30, v237, 14
	v_writelane_b32 v236, s11, 50
	v_cmp_lt_u32_e64 s[10:11], v1, v100
	v_or_b32_e32 v1, 11, v3
	v_cmp_eq_u32_e64 s[60:61], v1, v100
	v_writelane_b32 v236, s10, 51
	v_cmp_lt_u32_e64 s[54:55], v100, v1
	v_cmp_lt_u32_e64 s[56:57], v1, v100
	v_or_b32_e32 v1, 17, v3
	v_writelane_b32 v236, s11, 52
	v_cmp_lt_u32_e64 s[10:11], v8, v100
	v_or_b32_e32 v8, 10, v3
	v_cmp_eq_u32_e64 s[68:69], v1, v100
	v_cmp_lt_u32_e64 s[62:63], v100, v1
	v_cmp_lt_u32_e64 s[64:65], v1, v100
	v_or_b32_e32 v1, 19, v3
	v_cmp_lt_u32_e64 s[52:53], v100, v8
	v_cmp_eq_u32_e32 vcc, v8, v100
	v_cmp_lt_u32_e64 s[58:59], v8, v100
	v_or_b32_e32 v8, 16, v3
	v_cmp_eq_u32_e64 s[76:77], v1, v100
	v_cmp_lt_u32_e64 s[70:71], v100, v1
	v_cmp_lt_u32_e64 s[72:73], v1, v100
	v_or_b32_e32 v1, 25, v3
	v_writelane_b32 v236, s10, 53
	v_cndmask_b32_e64 v111, 0, 1.0, s[60:61]
	v_cndmask_b32_e64 v110, 0, 1.0, vcc
	v_cmp_lt_u32_e64 s[60:61], v100, v8
	v_cmp_eq_u32_e32 vcc, v8, v100
	v_cmp_lt_u32_e64 s[66:67], v8, v100
	v_or_b32_e32 v8, 18, v3
	v_cmp_eq_u32_e64 s[84:85], v1, v100
	v_cmp_lt_u32_e64 s[78:79], v100, v1
	v_cmp_lt_u32_e64 s[80:81], v1, v100
	v_or_b32_e32 v1, 27, v3
	v_writelane_b32 v236, s11, 54
	v_cndmask_b32_e64 v113, 0, 1.0, s[68:69]
	v_cndmask_b32_e64 v112, 0, 1.0, vcc
	v_cmp_lt_u32_e64 s[68:69], v100, v8
	v_cmp_eq_u32_e32 vcc, v8, v100
	v_cmp_lt_u32_e64 s[74:75], v8, v100
	v_or_b32_e32 v8, 24, v3
	v_cmp_eq_u32_e64 s[92:93], v1, v100
	v_cmp_lt_u32_e64 s[86:87], v100, v1
	v_cmp_lt_u32_e64 s[88:89], v1, v100
	v_or_b32_e32 v1, 16, v2
	v_readlane_b32 s31, v237, 15
	v_mul_u32_u24_e32 v16, 0x50, v15
	v_cndmask_b32_e64 v115, 0, 1.0, s[76:77]
	v_cndmask_b32_e64 v114, 0, 1.0, vcc
	v_cmp_lt_u32_e64 s[76:77], v100, v8
	v_cmp_eq_u32_e32 vcc, v8, v100
	v_cmp_lt_u32_e64 s[82:83], v8, v100
	v_mul_u32_u24_e32 v8, 0x50, v1
	v_sub_u32_e32 v1, 0x8ff, v0
	v_writelane_b32 v236, s0, 55
	v_readlane_b32 s17, v237, 1
	v_and_b32_e32 v7, 28, v163
	v_add3_u32 v171, 0, v16, v17
	v_cmp_lt_u32_e64 s[30:31], v3, v100
	v_or_b32_e32 v3, 26, v3
	v_lshrrev_b32_e32 v50, 8, v1
	v_writelane_b32 v236, s1, 56
	s_lshl_b32 s0, s4, 2
	v_readlane_b32 s21, v237, 5
	v_lshl_add_u32 v7, v7, 1, 0
	v_lshl_add_u32 v172, s4, 1, v171
	v_add_u32_e32 v175, v13, v14
	v_add_u32_e32 v10, s15, v14
	v_mul_u32_u24_e32 v13, 0x50, v2
	v_mul_u32_u24_e32 v6, 0x50, v94
	v_cmp_lt_u32_e64 s[14:15], v11, v9
	v_cmp_gt_u32_e64 s[16:17], v11, v9
	v_cndmask_b32_e64 v117, 0, 1.0, s[84:85]
	v_cndmask_b32_e64 v116, 0, 1.0, vcc
	v_cmp_lt_u32_e64 s[84:85], v100, v3
	v_cmp_eq_u32_e32 vcc, v3, v100
	v_cmp_lt_u32_e64 s[90:91], v3, v100
	v_mul_u32_u24_e32 v3, 0x90, v2
	v_add_u32_e32 v1, 4, v50
	v_lshl_add_u32 v9, v0, 1, 0
	v_writelane_b32 v236, s0, 57
	v_readlane_b32 s4, v237, 61
	v_lshlrev_b32_e32 v53, 2, v2
	v_cmp_lt_u32_e64 s[36:37], 15, v0
	v_cmp_eq_u32_e64 s[6:7], 0, v162
	v_bfe_u32 v95, v0, 3, 1
	v_add_u32_e32 v179, s12, v14
	v_add_u32_e32 v181, 0xffffff00, v180
	v_add_u32_e32 v184, 0xffffff00, v183
	v_cndmask_b32_e64 v107, 0, 1.0, s[44:45]
	v_cndmask_b32_e64 v119, 0, 1.0, s[92:93]
	v_cndmask_b32_e64 v118, 0, 1.0, vcc
	v_and_b32_e32 v187, 28, v1
	v_mov_b32_e32 v1, v50
	v_mov_b32_e32 v52, v50
	v_mov_b32_e32 v51, v50
	v_add_u32_e32 v188, 0x5200, v9
	s_movk_i32 s33, 0x5400
	v_lshlrev_b32_e32 v120, 2, v4
	s_add_i32 s12, 0, 0x20040
	v_lshlrev_b32_e32 v122, 2, v2
	v_add_u32_e32 v189, v5, v4
	v_add_u32_e32 v190, v10, v13
	v_add_u32_e32 v191, v12, v3
	v_add_u32_e32 v192, v10, v8
	v_mov_b32_e32 v193, 0x5400
	v_add_u32_e32 v194, v7, v6
	s_mov_b32 s40, s4
	s_mov_b32 s21, 0
	v_writelane_b32 v236, s38, 58
	v_readlane_b32 s18, v237, 2
	v_readlane_b32 s19, v237, 3
	v_readlane_b32 s20, v237, 4
	v_readlane_b32 s5, v237, 62
	v_writelane_b32 v236, s39, 59
	s_setprio 1
	s_branch .LBB0_968

; #define LAS __attribute__((address_space(3)))
; #define CV_CLAIM(b_) do { b_ = 0xffffffffu; if (F.lane == 0) { if (!(p1done && __hip_atomic_load(p1done, __ATOMIC_RELAXED, __HIP_MEMORY_SCOPE_AGENT) >= ngemm)) b_ = __hip_atomic_fetch_add(next, 2u, __ATOMIC_RELAXED, __HIP_MEMORY_SCOPE_AGENT); } } while (0)
; __device__ __forceinline__ void convert_loop(Frame& F, unsigned* next, unsigned* p1done, unsigned ngemm, LAS unsigned char* cvbuf, unsigned lo, unsigned hi) {
;     ...
;     unsigned nb; CV_CLAIM(nb);
;     for (;;) { const unsigned b0 = (unsigned)__builtin_amdgcn_readfirstlane((int)nb); if (b0 >= hi - lo) break;
;         const unsigned base = b0 + lo;
;         if (!p1done) CV_CLAIM(nb);
; __global__ void __launch_bounds__(NTHR, 2) mk_fwd(Args args) {
;     ...
;           if (F.wave >= CV_W0) convert_loop(F, F.ctl + CW_CVNEXT, nullptr, 0u, F.lds + 45056 + (F.wave - 4) * 9216, 0u, (unsigned)CV_SPLIT);
.LBB0_1058:
	s_setprio 0
	v_readlane_b32 s93, v236, 30
	v_readlane_b32 s76, v237, 63
	v_readlane_b32 s64, v237, 59
	s_cmpk_lt_u32 s93, 0x180
	v_readlane_b32 s77, v236, 0
	v_readlane_b32 s78, v236, 1
	v_readlane_b32 s79, v236, 2
	v_readlane_b32 s80, v236, 3
	v_readlane_b32 s81, v236, 4
	v_readlane_b32 s82, v236, 5
	v_readlane_b32 s83, v236, 6
	v_readlane_b32 s84, v236, 7
	v_readlane_b32 s85, v236, 8
	v_readlane_b32 s86, v236, 9
	v_readlane_b32 s87, v236, 10
	v_readlane_b32 s88, v236, 11
	v_readlane_b32 s89, v236, 12
	v_readlane_b32 s90, v236, 13
	v_readlane_b32 s91, v236, 14
	v_readlane_b32 s74, v237, 61
	s_mov_b32 s72, s64
	v_readlane_b32 s92, v236, 27
	v_readlane_b32 s75, v237, 62
	v_readlane_b32 s65, v237, 60
	s_cbranch_scc1 .LBB0_1096
	s_add_u32 s0, s90, 0x8000
	s_addc_u32 s1, s91, 0
	v_cmp_eq_u32_e64 s[4:5], 0, v162
	v_mov_b32_e32 v1, -1
	s_and_saveexec_b64 s[2:3], s[4:5]
	s_cbranch_execz .LBB0_1063
	s_mov_b64 s[8:9], exec
	v_mbcnt_lo_u32_b32 v1, s8, 0
	v_mbcnt_hi_u32_b32 v1, s9, v1
	v_cmp_eq_u32_e32 vcc, 0, v1
	s_and_saveexec_b64 s[6:7], vcc
	s_cbranch_execz .LBB0_1062
	s_bcnt1_i32_b64 s8, s[8:9]
	s_lshl_b32 s8, s8, 1
	s_waitcnt vmcnt(4)
	v_mov_b32_e32 v2, 0
	v_mov_b32_e32 v3, s8
	global_atomic_add v2, v2, v3, s[0:1] sc0
